# baseline (speedup 1.0000x reference)
_Z8gemm_f16ILi128ELi64ELi2ELi2ELi4ELi2ELi0EEvPKDF16_S1_Pviiii:
	s_load_dwordx4 s[4:7], s[0:1], 0x0
	s_load_dwordx2 s[8:9], s[0:1], 0x10
	s_and_b32 s3, s2, 7
	s_lshr_b32 s10, s2, 3
	s_lshr_b32 s11, s3, 1
	s_lshl_b32 s11, s11, 2
	s_and_b32 s12, s10, 3
	s_and_b32 s3, s3, 1
	s_lshl_b32 s3, s3, 3
	s_lshr_b32 s10, s10, 2
	s_add_i32 s10, s10, s3
	s_add_i32 s3, s11, s12
	s_mov_b32 s11, s10
	s_lshl_b32 s10, s3, 7
	s_lshl_b32 s11, s11, 6
	v_lshrrev_b32_e32 v13, 3, v0
	v_and_b32_e32 v14, 7, v0
	v_bfe_u32 v15, v0, 4, 3
	v_xor_b32_e32 v14, v14, v15
	v_lshlrev_b32_e32 v14, 4, v14
	v_add_u32_e32 v15, s10, v13
	v_mul_u32_u24_e32 v15, 0xc00, v15
	v_add_u32_e32 v3, v15, v14
	v_add_u32_e32 v4, 0x18000, v3
	v_add_u32_e32 v5, 0x30000, v3
	v_add_u32_e32 v6, 0x48000, v3
	v_add_u32_e32 v15, s11, v13
	v_mul_u32_u24_e32 v15, 0xc00, v15
	v_add_u32_e32 v7, v15, v14
	v_add_u32_e32 v8, 0x18000, v7
	v_lshlrev_b32_e32 v13, 4, v0
	s_nop 0
	v_readfirstlane_b32 s20, v13
	v_and_b32_e32 v13, 15, v0
	v_bfe_u32 v14, v0, 4, 2
	v_bfe_u32 v15, v0, 1, 3
	v_xor_b32_e32 v14, v14, v15
	v_lshlrev_b32_e32 v14, 4, v14
	v_lshl_or_b32 v14, v13, 7, v14
	v_lshrrev_b32_e32 v13, 7, v0
	v_lshl_or_b32 v1, v13, 13, v14
	v_bfe_u32 v13, v0, 6, 1
	v_lshlrev_b32_e32 v13, 12, v13
	v_or_b32_e32 v13, 0x4000, v13
	v_or_b32_e32 v2, v13, v14
	s_waitcnt lgkmcnt(0)
	s_mov_b32 s14, s4
	s_mov_b32 s15, s5
	s_mov_b32 s16, s6
	s_mov_b32 s17, s7
	s_mov_b32 s21, s20
	s_mov_b32 m0, s21
	s_add_i32 s21, s21, 0x1000
	global_load_lds_dwordx4 v3, s[14:15]
	s_mov_b32 m0, s21
	s_add_i32 s21, s21, 0x1000
	global_load_lds_dwordx4 v4, s[14:15]
	s_mov_b32 m0, s21
	s_add_i32 s21, s21, 0x1000
	global_load_lds_dwordx4 v5, s[14:15]
	s_mov_b32 m0, s21
	s_add_i32 s21, s21, 0x1000
	global_load_lds_dwordx4 v6, s[14:15]
	s_mov_b32 m0, s21
	s_add_i32 s21, s21, 0x1000
	global_load_lds_dwordx4 v7, s[16:17]
	s_mov_b32 m0, s21
	s_add_i32 s21, s21, 0x1000
	global_load_lds_dwordx4 v8, s[16:17]
	s_add_u32 s14, s14, 0x80
	s_addc_u32 s15, s15, 0
	s_add_u32 s16, s16, 0x80
	s_addc_u32 s17, s17, 0
	s_mov_b32 m0, s21
	s_add_i32 s21, s21, 0x1000
	global_load_lds_dwordx4 v3, s[14:15]
	s_mov_b32 m0, s21
	s_add_i32 s21, s21, 0x1000
	global_load_lds_dwordx4 v4, s[14:15]
	s_mov_b32 m0, s21
	s_add_i32 s21, s21, 0x1000
	global_load_lds_dwordx4 v5, s[14:15]
	s_mov_b32 m0, s21
	s_add_i32 s21, s21, 0x1000
	global_load_lds_dwordx4 v6, s[14:15]
	s_mov_b32 m0, s21
	s_add_i32 s21, s21, 0x1000
	global_load_lds_dwordx4 v7, s[16:17]
	s_mov_b32 m0, s21
	s_add_i32 s21, s21, 0x1000
	global_load_lds_dwordx4 v8, s[16:17]
	s_add_u32 s14, s14, 0x80
	s_addc_u32 s15, s15, 0
	s_add_u32 s16, s16, 0x80
	s_addc_u32 s17, s17, 0
	s_mov_b32 m0, s21
	s_add_i32 s21, s21, 0x1000
	global_load_lds_dwordx4 v3, s[14:15]
	s_mov_b32 m0, s21
	s_add_i32 s21, s21, 0x1000
	global_load_lds_dwordx4 v4, s[14:15]
	s_mov_b32 m0, s21
	s_add_i32 s21, s21, 0x1000
	global_load_lds_dwordx4 v5, s[14:15]
	s_mov_b32 m0, s21
	s_add_i32 s21, s21, 0x1000
	global_load_lds_dwordx4 v6, s[14:15]
	s_mov_b32 m0, s21
	s_add_i32 s21, s21, 0x1000
	global_load_lds_dwordx4 v7, s[16:17]
	s_mov_b32 m0, s21
	s_add_i32 s21, s21, 0x1000
	global_load_lds_dwordx4 v8, s[16:17]
	s_add_u32 s14, s14, 0x80
	s_addc_u32 s15, s15, 0
	s_add_u32 s16, s16, 0x80
	s_addc_u32 s17, s17, 0
	s_mov_b32 m0, s21
	s_add_i32 s21, s21, 0x1000
	global_load_lds_dwordx4 v3, s[14:15]
	s_mov_b32 m0, s21
	s_add_i32 s21, s21, 0x1000
	global_load_lds_dwordx4 v4, s[14:15]
	s_mov_b32 m0, s21
	s_add_i32 s21, s21, 0x1000
	global_load_lds_dwordx4 v5, s[14:15]
	s_mov_b32 m0, s21
	s_add_i32 s21, s21, 0x1000
	global_load_lds_dwordx4 v6, s[14:15]
	s_mov_b32 m0, s21
	s_add_i32 s21, s21, 0x1000
	global_load_lds_dwordx4 v7, s[16:17]
	s_mov_b32 m0, s21
	s_add_i32 s21, s21, 0x1000
	global_load_lds_dwordx4 v8, s[16:17]
	v_accvgpr_write_b32 a0, 0
	v_accvgpr_write_b32 a1, 0
	v_accvgpr_write_b32 a2, 0
	v_accvgpr_write_b32 a3, 0
	v_accvgpr_write_b32 a4, 0
	v_accvgpr_write_b32 a5, 0
	v_accvgpr_write_b32 a6, 0
	v_accvgpr_write_b32 a7, 0
	v_accvgpr_write_b32 a8, 0
	v_accvgpr_write_b32 a9, 0
	v_accvgpr_write_b32 a10, 0
	v_accvgpr_write_b32 a11, 0
	v_accvgpr_write_b32 a12, 0
	v_accvgpr_write_b32 a13, 0
	v_accvgpr_write_b32 a14, 0
	v_accvgpr_write_b32 a15, 0
	v_accvgpr_write_b32 a16, 0
	v_accvgpr_write_b32 a17, 0
	v_accvgpr_write_b32 a18, 0
	v_accvgpr_write_b32 a19, 0
	v_accvgpr_write_b32 a20, 0
	v_accvgpr_write_b32 a21, 0
	v_accvgpr_write_b32 a22, 0
	v_accvgpr_write_b32 a23, 0
	v_accvgpr_write_b32 a24, 0
	v_accvgpr_write_b32 a25, 0
	v_accvgpr_write_b32 a26, 0
	v_accvgpr_write_b32 a27, 0
	v_accvgpr_write_b32 a28, 0
	v_accvgpr_write_b32 a29, 0
	v_accvgpr_write_b32 a30, 0
	v_accvgpr_write_b32 a31, 0
	s_mov_b32 s12, 0
	s_mov_b32 s13, 0
	v_mov_b32_e32 v9, v1
	v_mov_b32_e32 v11, v2
	v_xor_b32_e32 v10, 64, v1
	v_xor_b32_e32 v12, 64, v2
	s_waitcnt vmcnt(18)
	s_barrier
	ds_read_b128 v[16:19], v11
	ds_read_b128 v[24:27], v9
	ds_read_b128 v[20:23], v11 offset:2048
	ds_read_b128 v[28:31], v9 offset:2048
	ds_read_b128 v[32:35], v9 offset:4096
	ds_read_b128 v[36:39], v9 offset:6144
	s_add_i32 s23, s13, 0x6000
	s_cmp_lg_u32 s23, 0x18000
	s_cselect_b32 s23, s23, 0
	s_waitcnt lgkmcnt(0)
	v_mfma_f32_16x16x32_f16 a[0:3], v[16:19], v[24:27], a[0:3]
	ds_read_b128 v[40:43], v12
	v_mfma_f32_16x16x32_f16 a[4:7], v[20:23], v[24:27], a[4:7]
	ds_read_b128 v[48:51], v10
	v_mfma_f32_16x16x32_f16 a[8:11], v[16:19], v[28:31], a[8:11]
	ds_read_b128 v[44:47], v12 offset:2048
	v_mfma_f32_16x16x32_f16 a[12:15], v[20:23], v[28:31], a[12:15]
	ds_read_b128 v[52:55], v10 offset:2048
	v_mfma_f32_16x16x32_f16 a[16:19], v[16:19], v[32:35], a[16:19]
	ds_read_b128 v[56:59], v10 offset:4096
	v_mfma_f32_16x16x32_f16 a[20:23], v[20:23], v[32:35], a[20:23]
	ds_read_b128 v[60:63], v10 offset:6144
	v_mfma_f32_16x16x32_f16 a[24:27], v[16:19], v[36:39], a[24:27]
	v_add_u32_e32 v9, s23, v1
	v_add_u32_e32 v11, s23, v2
	v_mfma_f32_16x16x32_f16 a[28:31], v[20:23], v[36:39], a[28:31]
	v_xor_b32_e32 v10, 64, v9
	v_xor_b32_e32 v12, 64, v11
	s_waitcnt vmcnt(12)
	s_waitcnt lgkmcnt(0)
	s_barrier
	s_add_i32 s22, s12, 4
	s_lshl_b32 s22, s22, 7
	s_add_u32 s14, s4, s22
	s_addc_u32 s15, s5, 0
	s_add_u32 s16, s6, s22
	s_addc_u32 s17, s7, 0
	s_add_i32 s21, s13, s20
	v_mfma_f32_16x16x32_f16 a[0:3], v[40:43], v[48:51], a[0:3]
	ds_read_b128 v[16:19], v11
	v_mfma_f32_16x16x32_f16 a[4:7], v[44:47], v[48:51], a[4:7]
	ds_read_b128 v[24:27], v9
	s_mov_b32 m0, s21
	s_add_i32 s21, s21, 0x1000
	global_load_lds_dwordx4 v3, s[14:15]
	v_mfma_f32_16x16x32_f16 a[8:11], v[40:43], v[52:55], a[8:11]
	ds_read_b128 v[20:23], v11 offset:2048
	v_mfma_f32_16x16x32_f16 a[12:15], v[44:47], v[52:55], a[12:15]
	ds_read_b128 v[28:31], v9 offset:2048
	v_mfma_f32_16x16x32_f16 a[16:19], v[40:43], v[56:59], a[16:19]
	ds_read_b128 v[32:35], v9 offset:4096
	s_mov_b32 m0, s21
	s_add_i32 s21, s21, 0x1000
	global_load_lds_dwordx4 v4, s[14:15]
	v_mfma_f32_16x16x32_f16 a[20:23], v[44:47], v[56:59], a[20:23]
	ds_read_b128 v[36:39], v9 offset:6144
	v_mfma_f32_16x16x32_f16 a[24:27], v[40:43], v[60:63], a[24:27]
	v_mfma_f32_16x16x32_f16 a[28:31], v[44:47], v[60:63], a[28:31]
	s_mov_b32 m0, s21
	s_add_i32 s21, s21, 0x1000
	global_load_lds_dwordx4 v5, s[14:15]
	s_mov_b32 s13, s23
	s_add_i32 s12, s12, 1
.Lg2_loop:
	s_add_i32 s23, s13, 0x6000
	s_cmp_lg_u32 s23, 0x18000
	s_cselect_b32 s23, s23, 0
	s_waitcnt lgkmcnt(0)
	v_mfma_f32_16x16x32_f16 a[0:3], v[16:19], v[24:27], a[0:3]
	ds_read_b128 v[40:43], v12
	v_mfma_f32_16x16x32_f16 a[4:7], v[20:23], v[24:27], a[4:7]
	ds_read_b128 v[48:51], v10
	s_mov_b32 m0, s21
	s_add_i32 s21, s21, 0x1000
	global_load_lds_dwordx4 v6, s[14:15]
	v_mfma_f32_16x16x32_f16 a[8:11], v[16:19], v[28:31], a[8:11]
	ds_read_b128 v[44:47], v12 offset:2048
	v_mfma_f32_16x16x32_f16 a[12:15], v[20:23], v[28:31], a[12:15]
	ds_read_b128 v[52:55], v10 offset:2048
	v_mfma_f32_16x16x32_f16 a[16:19], v[16:19], v[32:35], a[16:19]
	ds_read_b128 v[56:59], v10 offset:4096
	s_mov_b32 m0, s21
	s_add_i32 s21, s21, 0x1000
	global_load_lds_dwordx4 v7, s[16:17]
	v_mfma_f32_16x16x32_f16 a[20:23], v[20:23], v[32:35], a[20:23]
	ds_read_b128 v[60:63], v10 offset:6144
	v_mfma_f32_16x16x32_f16 a[24:27], v[16:19], v[36:39], a[24:27]
	v_add_u32_e32 v9, s23, v1
	v_add_u32_e32 v11, s23, v2
	s_mov_b32 m0, s21
	s_nop 0
	global_load_lds_dwordx4 v8, s[16:17]
	v_mfma_f32_16x16x32_f16 a[28:31], v[20:23], v[36:39], a[28:31]
	v_xor_b32_e32 v10, 64, v9
	v_xor_b32_e32 v12, 64, v11
	s_waitcnt vmcnt(12)
	s_waitcnt lgkmcnt(0)
	s_barrier
	s_add_i32 s22, s12, 4
	s_lshl_b32 s22, s22, 7
	s_add_u32 s14, s4, s22
	s_addc_u32 s15, s5, 0
	s_add_u32 s16, s6, s22
	s_addc_u32 s17, s7, 0
	s_add_i32 s21, s13, s20
	v_mfma_f32_16x16x32_f16 a[0:3], v[40:43], v[48:51], a[0:3]
	ds_read_b128 v[16:19], v11
	v_mfma_f32_16x16x32_f16 a[4:7], v[44:47], v[48:51], a[4:7]
	ds_read_b128 v[24:27], v9
	s_mov_b32 m0, s21
	s_add_i32 s21, s21, 0x1000
	global_load_lds_dwordx4 v3, s[14:15]
	v_mfma_f32_16x16x32_f16 a[8:11], v[40:43], v[52:55], a[8:11]
	ds_read_b128 v[20:23], v11 offset:2048
	v_mfma_f32_16x16x32_f16 a[12:15], v[44:47], v[52:55], a[12:15]
	ds_read_b128 v[28:31], v9 offset:2048
	v_mfma_f32_16x16x32_f16 a[16:19], v[40:43], v[56:59], a[16:19]
	ds_read_b128 v[32:35], v9 offset:4096
	s_mov_b32 m0, s21
	s_add_i32 s21, s21, 0x1000
	global_load_lds_dwordx4 v4, s[14:15]
	v_mfma_f32_16x16x32_f16 a[20:23], v[44:47], v[56:59], a[20:23]
	ds_read_b128 v[36:39], v9 offset:6144
	v_mfma_f32_16x16x32_f16 a[24:27], v[40:43], v[60:63], a[24:27]
	v_mfma_f32_16x16x32_f16 a[28:31], v[44:47], v[60:63], a[28:31]
	s_mov_b32 m0, s21
	s_add_i32 s21, s21, 0x1000
	global_load_lds_dwordx4 v5, s[14:15]
	s_mov_b32 s13, s23
	s_add_i32 s12, s12, 1
	s_cmp_lt_u32 s12, 20
	s_cbranch_scc1 .Lg2_loop
	s_add_i32 s23, s13, 0x6000
	s_cmp_lg_u32 s23, 0x18000
	s_cselect_b32 s23, s23, 0
	s_waitcnt lgkmcnt(0)
	v_mfma_f32_16x16x32_f16 a[0:3], v[16:19], v[24:27], a[0:3]
	ds_read_b128 v[40:43], v12
	v_mfma_f32_16x16x32_f16 a[4:7], v[20:23], v[24:27], a[4:7]
	ds_read_b128 v[48:51], v10
	s_mov_b32 m0, s21
	s_add_i32 s21, s21, 0x1000
	global_load_lds_dwordx4 v6, s[14:15]
	v_mfma_f32_16x16x32_f16 a[8:11], v[16:19], v[28:31], a[8:11]
	ds_read_b128 v[44:47], v12 offset:2048
	v_mfma_f32_16x16x32_f16 a[12:15], v[20:23], v[28:31], a[12:15]
	ds_read_b128 v[52:55], v10 offset:2048
	v_mfma_f32_16x16x32_f16 a[16:19], v[16:19], v[32:35], a[16:19]
	ds_read_b128 v[56:59], v10 offset:4096
	s_mov_b32 m0, s21
	s_add_i32 s21, s21, 0x1000
	global_load_lds_dwordx4 v7, s[16:17]
	v_mfma_f32_16x16x32_f16 a[20:23], v[20:23], v[32:35], a[20:23]
	ds_read_b128 v[60:63], v10 offset:6144
	v_mfma_f32_16x16x32_f16 a[24:27], v[16:19], v[36:39], a[24:27]
	v_add_u32_e32 v9, s23, v1
	v_add_u32_e32 v11, s23, v2
	s_mov_b32 m0, s21
	s_nop 0
	global_load_lds_dwordx4 v8, s[16:17]
	v_mfma_f32_16x16x32_f16 a[28:31], v[20:23], v[36:39], a[28:31]
	v_xor_b32_e32 v10, 64, v9
	v_xor_b32_e32 v12, 64, v11
	s_waitcnt vmcnt(12)
	s_waitcnt lgkmcnt(0)
	s_barrier
	v_mfma_f32_16x16x32_f16 a[0:3], v[40:43], v[48:51], a[0:3]
	ds_read_b128 v[16:19], v11
	v_mfma_f32_16x16x32_f16 a[4:7], v[44:47], v[48:51], a[4:7]
	ds_read_b128 v[24:27], v9
	v_mfma_f32_16x16x32_f16 a[8:11], v[40:43], v[52:55], a[8:11]
	ds_read_b128 v[20:23], v11 offset:2048
	v_mfma_f32_16x16x32_f16 a[12:15], v[44:47], v[52:55], a[12:15]
	ds_read_b128 v[28:31], v9 offset:2048
	v_mfma_f32_16x16x32_f16 a[16:19], v[40:43], v[56:59], a[16:19]
	ds_read_b128 v[32:35], v9 offset:4096
	v_mfma_f32_16x16x32_f16 a[20:23], v[44:47], v[56:59], a[20:23]
	ds_read_b128 v[36:39], v9 offset:6144
	v_mfma_f32_16x16x32_f16 a[24:27], v[40:43], v[60:63], a[24:27]
	v_mfma_f32_16x16x32_f16 a[28:31], v[44:47], v[60:63], a[28:31]
	s_mov_b32 s13, s23
	s_add_i32 s12, s12, 1
	s_add_i32 s23, s13, 0x6000
	s_cmp_lg_u32 s23, 0x18000
	s_cselect_b32 s23, s23, 0
	s_waitcnt lgkmcnt(0)
	v_mfma_f32_16x16x32_f16 a[0:3], v[16:19], v[24:27], a[0:3]
	ds_read_b128 v[40:43], v12
	v_mfma_f32_16x16x32_f16 a[4:7], v[20:23], v[24:27], a[4:7]
	ds_read_b128 v[48:51], v10
	v_mfma_f32_16x16x32_f16 a[8:11], v[16:19], v[28:31], a[8:11]
	ds_read_b128 v[44:47], v12 offset:2048
	v_mfma_f32_16x16x32_f16 a[12:15], v[20:23], v[28:31], a[12:15]
	ds_read_b128 v[52:55], v10 offset:2048
	v_mfma_f32_16x16x32_f16 a[16:19], v[16:19], v[32:35], a[16:19]
	ds_read_b128 v[56:59], v10 offset:4096
	v_mfma_f32_16x16x32_f16 a[20:23], v[20:23], v[32:35], a[20:23]
	ds_read_b128 v[60:63], v10 offset:6144
	v_mfma_f32_16x16x32_f16 a[24:27], v[16:19], v[36:39], a[24:27]
	v_add_u32_e32 v9, s23, v1
	v_add_u32_e32 v11, s23, v2
	v_mfma_f32_16x16x32_f16 a[28:31], v[20:23], v[36:39], a[28:31]
	v_xor_b32_e32 v10, 64, v9
	v_xor_b32_e32 v12, 64, v11
	s_waitcnt vmcnt(6)
	s_waitcnt lgkmcnt(0)
	s_barrier
	v_mfma_f32_16x16x32_f16 a[0:3], v[40:43], v[48:51], a[0:3]
	ds_read_b128 v[16:19], v11
	v_mfma_f32_16x16x32_f16 a[4:7], v[44:47], v[48:51], a[4:7]
	ds_read_b128 v[24:27], v9
	v_mfma_f32_16x16x32_f16 a[8:11], v[40:43], v[52:55], a[8:11]
	ds_read_b128 v[20:23], v11 offset:2048
	v_mfma_f32_16x16x32_f16 a[12:15], v[44:47], v[52:55], a[12:15]
	ds_read_b128 v[28:31], v9 offset:2048
	v_mfma_f32_16x16x32_f16 a[16:19], v[40:43], v[56:59], a[16:19]
	ds_read_b128 v[32:35], v9 offset:4096
	v_mfma_f32_16x16x32_f16 a[20:23], v[44:47], v[56:59], a[20:23]
	ds_read_b128 v[36:39], v9 offset:6144
	v_mfma_f32_16x16x32_f16 a[24:27], v[40:43], v[60:63], a[24:27]
	v_mfma_f32_16x16x32_f16 a[28:31], v[44:47], v[60:63], a[28:31]
	s_mov_b32 s13, s23
	s_add_i32 s12, s12, 1
	s_add_i32 s23, s13, 0x6000
	s_cmp_lg_u32 s23, 0x18000
	s_cselect_b32 s23, s23, 0
	s_waitcnt lgkmcnt(0)
	v_mfma_f32_16x16x32_f16 a[0:3], v[16:19], v[24:27], a[0:3]
	ds_read_b128 v[40:43], v12
	v_mfma_f32_16x16x32_f16 a[4:7], v[20:23], v[24:27], a[4:7]
	ds_read_b128 v[48:51], v10
	v_mfma_f32_16x16x32_f16 a[8:11], v[16:19], v[28:31], a[8:11]
	ds_read_b128 v[44:47], v12 offset:2048
	v_mfma_f32_16x16x32_f16 a[12:15], v[20:23], v[28:31], a[12:15]
	ds_read_b128 v[52:55], v10 offset:2048
	v_mfma_f32_16x16x32_f16 a[16:19], v[16:19], v[32:35], a[16:19]
	ds_read_b128 v[56:59], v10 offset:4096
	v_mfma_f32_16x16x32_f16 a[20:23], v[20:23], v[32:35], a[20:23]
	ds_read_b128 v[60:63], v10 offset:6144
	v_mfma_f32_16x16x32_f16 a[24:27], v[16:19], v[36:39], a[24:27]
	v_add_u32_e32 v9, s23, v1
	v_add_u32_e32 v11, s23, v2
	v_mfma_f32_16x16x32_f16 a[28:31], v[20:23], v[36:39], a[28:31]
	v_xor_b32_e32 v10, 64, v9
	v_xor_b32_e32 v12, 64, v11
	s_waitcnt vmcnt(0)
	s_waitcnt lgkmcnt(0)
	s_barrier
	v_mfma_f32_16x16x32_f16 a[0:3], v[40:43], v[48:51], a[0:3]
	ds_read_b128 v[16:19], v11
	v_mfma_f32_16x16x32_f16 a[4:7], v[44:47], v[48:51], a[4:7]
	ds_read_b128 v[24:27], v9
	v_mfma_f32_16x16x32_f16 a[8:11], v[40:43], v[52:55], a[8:11]
	ds_read_b128 v[20:23], v11 offset:2048
	v_mfma_f32_16x16x32_f16 a[12:15], v[44:47], v[52:55], a[12:15]
	ds_read_b128 v[28:31], v9 offset:2048
	v_mfma_f32_16x16x32_f16 a[16:19], v[40:43], v[56:59], a[16:19]
	ds_read_b128 v[32:35], v9 offset:4096
	v_mfma_f32_16x16x32_f16 a[20:23], v[44:47], v[56:59], a[20:23]
	ds_read_b128 v[36:39], v9 offset:6144
	v_mfma_f32_16x16x32_f16 a[24:27], v[40:43], v[60:63], a[24:27]
	v_mfma_f32_16x16x32_f16 a[28:31], v[44:47], v[60:63], a[28:31]
	s_mov_b32 s13, s23
	s_add_i32 s12, s12, 1
	s_add_i32 s23, s13, 0x6000
	s_cmp_lg_u32 s23, 0x18000
	s_cselect_b32 s23, s23, 0
	s_waitcnt lgkmcnt(0)
	v_mfma_f32_16x16x32_f16 a[0:3], v[16:19], v[24:27], a[0:3]
	ds_read_b128 v[40:43], v12
	v_mfma_f32_16x16x32_f16 a[4:7], v[20:23], v[24:27], a[4:7]
	ds_read_b128 v[48:51], v10
	v_mfma_f32_16x16x32_f16 a[8:11], v[16:19], v[28:31], a[8:11]
	ds_read_b128 v[44:47], v12 offset:2048
	v_mfma_f32_16x16x32_f16 a[12:15], v[20:23], v[28:31], a[12:15]
	ds_read_b128 v[52:55], v10 offset:2048
	v_mfma_f32_16x16x32_f16 a[16:19], v[16:19], v[32:35], a[16:19]
	ds_read_b128 v[56:59], v10 offset:4096
	v_mfma_f32_16x16x32_f16 a[20:23], v[20:23], v[32:35], a[20:23]
	ds_read_b128 v[60:63], v10 offset:6144
	v_mfma_f32_16x16x32_f16 a[24:27], v[16:19], v[36:39], a[24:27]
	v_add_u32_e32 v9, s23, v1
	v_add_u32_e32 v11, s23, v2
	v_mfma_f32_16x16x32_f16 a[28:31], v[20:23], v[36:39], a[28:31]
	v_xor_b32_e32 v10, 64, v9
	v_xor_b32_e32 v12, 64, v11
	s_waitcnt lgkmcnt(0)
	s_barrier
	v_mfma_f32_16x16x32_f16 a[0:3], v[40:43], v[48:51], a[0:3]
	ds_read_b128 v[16:19], v11
	v_mfma_f32_16x16x32_f16 a[4:7], v[44:47], v[48:51], a[4:7]
	ds_read_b128 v[24:27], v9
	v_mfma_f32_16x16x32_f16 a[8:11], v[40:43], v[52:55], a[8:11]
	ds_read_b128 v[20:23], v11 offset:2048
	v_mfma_f32_16x16x32_f16 a[12:15], v[44:47], v[52:55], a[12:15]
	ds_read_b128 v[28:31], v9 offset:2048
	v_mfma_f32_16x16x32_f16 a[16:19], v[40:43], v[56:59], a[16:19]
	ds_read_b128 v[32:35], v9 offset:4096
	v_mfma_f32_16x16x32_f16 a[20:23], v[44:47], v[56:59], a[20:23]
	ds_read_b128 v[36:39], v9 offset:6144
	v_mfma_f32_16x16x32_f16 a[24:27], v[40:43], v[60:63], a[24:27]
	v_mfma_f32_16x16x32_f16 a[28:31], v[44:47], v[60:63], a[28:31]
	s_mov_b32 s13, s23
	s_add_i32 s12, s12, 1
	s_waitcnt vmcnt(0) lgkmcnt(0)
	v_and_b32_e32 v13, 15, v0
	v_lshrrev_b32_e32 v14, 7, v0
	v_lshl_add_u32 v13, v14, 6, v13
	v_add_u32_e32 v13, s10, v13
	v_bfe_u32 v14, v0, 6, 1
	v_bfe_u32 v15, v0, 4, 2
	v_lshlrev_b32_e32 v14, 5, v14
	v_lshl_add_u32 v14, v15, 2, v14
	v_add_u32_e32 v14, s11, v14
	v_lshlrev_b32_e32 v13, 10, v13
	v_add_u32_e32 v13, v13, v14
	v_lshlrev_b32_e32 v13, 2, v13
	v_add_u32_e32 v14, 0x10000, v13
	v_add_u32_e32 v15, 0x20000, v13
	v_add_u32_e32 v16, 0x30000, v13
	s_nop 7
	global_store_dwordx4 v13, a[0:3], s[8:9]
	global_store_dwordx4 v13, a[4:7], s[8:9] offset:64
	global_store_dwordx4 v14, a[8:11], s[8:9]
	global_store_dwordx4 v14, a[12:15], s[8:9] offset:64
	global_store_dwordx4 v15, a[16:19], s[8:9]
	global_store_dwordx4 v15, a[20:23], s[8:9] offset:64
	global_store_dwordx4 v16, a[24:27], s[8:9]
	global_store_dwordx4 v16, a[28:31], s[8:9] offset:64
	s_endpgm
	.p2alignl 8, 3212836864
